# MoE gate/up GEMM K-loop also restructured to 16 fp8 MFMAs per barrier interval (on top of the MoE down restructure)
# speedup vs baseline: 1.0003x; 1.0003x over previous
; #define PG8_STAGE_A(bufoff, soff, voff) do { _Pragma("unroll") for (int _i = 0; _i < 2; ++_i) \
;         __builtin_amdgcn_raw_ptr_buffer_load_lds(rsA, (LAS void*)(lds + (bufoff) + ldsw + _i * 8192), 16, (voff)[_i], (soff), 0, 0); } while (0)
; #define PG8_STAGE_B(bufoff, soff) do { _Pragma("unroll") for (int _i = 0; _i < 2; ++_i) \
;         __builtin_amdgcn_raw_ptr_buffer_load_lds(rsB, (LAS void*)(lds + (bufoff) + ldsw + _i * 8192), 16, voffB[_i], (soff), 0, 0); } while (0)
; #define PG8_WAIT_V(n) asm volatile("s_waitcnt vmcnt(" #n ")" ::: "memory")
; #define PG8_BAR __builtin_amdgcn_s_barrier()
; template <class Epi, class Sched, bool GATHER, bool ALIGN_EPI, bool SP2, bool FP8>
; __device__ __forceinline__ void gemm_phase(LAS unsigned char* lds, const Gemm g, const Sched& S, const Epi& E) {
;     ...
;         PG8_WAIT_V(4); PG8_BAR;
;         PG8_STAGE_B(PG8_SB(1, 0), cB + kstep); PG8_STAGE_A(PG8_SA(1, 0), cA + kstep, vA0); PG8_STAGE_B(PG8_SB(1, 1), cB + hstep + kstep);
;         PG8_WAIT_V(6); PG8_BAR;
.LBB0_923:
	s_add_u32 s26, s96, 0x3d800000
	s_addc_u32 s27, s97, 0
	s_add_u32 s28, s96, 0x500000
	s_addc_u32 s29, s97, 0
	s_add_i32 s44, s36, 0x18000
	s_or_b32 s1, s80, 0x80
	s_mov_b32 s66, s62
	s_mov_b32 s67, s63
	s_mov_b32 m0, s44
	s_add_i32 s45, s36, 0x1a000
	s_waitcnt vmcnt(2)
	s_barrier
	buffer_load_dwordx4 v173, s[64:67], s1 offen lds
	s_mov_b32 m0, s45
	s_add_i32 s46, s36, 0x8000
	buffer_load_dwordx4 v174, s[64:67], s1 offen lds
	s_mov_b32 m0, s46
	s_add_i32 s47, s36, 0xa000
	buffer_load_dwordx4 v183, s[60:63], s0 offen lds
	s_mov_b32 m0, s47
	s_add_i32 s48, s36, 0x1c000
	buffer_load_dwordx4 v185, s[60:63], s0 offen lds
	s_or_b32 s0, s80, 0x40080
	s_mov_b32 m0, s48
	s_add_i32 s49, s36, 0x1e000
	buffer_load_dwordx4 v173, s[64:67], s0 offen lds
	s_mov_b32 m0, s49
	v_lshlrev_b32_e32 v3, 6, v0
	buffer_load_dwordx4 v174, s[64:67], s0 offen lds
	v_and_b32_e32 v3, 0x3c0, v3
	v_lshlrev_b32_e32 v4, 2, v0
	v_lshl_or_b32 v3, v2, 1, v3
	s_lshl_b32 s0, s8, 13
	v_and_b32_e32 v4, 32, v4
	v_bitop3_b32 v5, s0, v3, v4 bitop3:0xf6
	s_lshl_b32 s0, s7, 5
	s_and_b32 s0, s0, 0x60
	v_mov_b32_e32 v18, 0
	s_lshl_b32 s1, s0, 7
	s_waitcnt vmcnt(6)
	s_add_i32 s51, s36, 0xc000
	v_mov_b32_e32 v20, v18
	v_mov_b32_e32 v21, v18
	v_bitop3_b32 v3, s1, v3, v4 bitop3:0xf6
	s_cmpk_lt_u32 s6, 0x100
	v_mov_b32_e32 v19, v18
	v_mov_b64_e32 v[32:33], v[20:21]
	v_mov_b64_e32 v[24:25], v[20:21]
	v_mov_b64_e32 v[28:29], v[20:21]
	s_cselect_b64 s[30:31], -1, 0
	s_add_i32 s52, s36, 0xe000
	s_ashr_i32 s53, s34, 31
	v_ashrrev_i32_e32 v165, 31, v164
	v_or_b32_e32 v175, s0, v2
	s_mov_b32 s56, 0
	s_add_i32 s57, 0, 0x27d04
	s_add_i32 s58, 0, 0x27d0c
	s_add_i32 s59, 0, 0x27d14
	s_add_i32 s83, 0, 0x27d1c
	s_add_i32 s93, 0, 0x27d24
	s_add_i32 s95, 0, 0x27d2c
	s_add_i32 s82, 0, 0x27d34
	s_add_i32 s92, 0, 0x27d3c
	s_add_i32 s20, 0, 0x27d44
	s_add_i32 s21, 0, 0x27d4c
	s_add_i32 s24, 0, 0x27d54
	s_add_i32 s68, 0, 0x27d5c
	s_add_i32 s69, 0, 0x27d64
	s_add_i32 s70, 0, 0x27d6c
	s_add_i32 s71, 0, 0x27d74
	s_add_i32 s72, 0, 0x27d7c
	v_add_u32_e32 v176, 0, v3
	v_add_u32_e32 v177, 0, v5
	s_mov_b32 s73, 0xc0e00000
	v_mov_b32_e32 v178, 0x40e00000
	v_mov_b64_e32 v[30:31], v[18:19]
	v_mov_b64_e32 v[22:23], v[18:19]
	v_mov_b64_e32 v[26:27], v[18:19]
	s_barrier
	s_branch .LBB0_926

; #define PG8_STAGE_A(bufoff, soff, voff) do { _Pragma("unroll") for (int _i = 0; _i < 2; ++_i) \
;         __builtin_amdgcn_raw_ptr_buffer_load_lds(rsA, (LAS void*)(lds + (bufoff) + ldsw + _i * 8192), 16, (voff)[_i], (soff), 0, 0); } while (0)
; #define PG8_STAGE_B(bufoff, soff) do { _Pragma("unroll") for (int _i = 0; _i < 2; ++_i) \
;         __builtin_amdgcn_raw_ptr_buffer_load_lds(rsB, (LAS void*)(lds + (bufoff) + ldsw + _i * 8192), 16, voffB[_i], (soff), 0, 0); } while (0)
; #define PG8_LDA(dst, b, h) do { _Pragma("unroll") for (int m = 0; m < 4; ++m) dst[m] = PG8_LD8(lds + PG8_SA(b, h) + aoff + m * 2048); } while (0)
; #define PG8_LDB(dst, b, h) do { _Pragma("unroll") for (int n = 0; n < 2; ++n) dst[n] = PG8_LD8(lds + PG8_SB(b, h) + boff + n * 2048); } while (0)
; #define PG8_WAIT_V(n) asm volatile("s_waitcnt vmcnt(" #n ")" ::: "memory")
; #define PG8_WAIT_L(n) asm volatile("s_waitcnt lgkmcnt(" #n ")" ::: "memory")
; #define PG8_BAR __builtin_amdgcn_s_barrier()
; #define PG8_SCHED __builtin_amdgcn_sched_barrier(0)
; template <class Epi, class Sched, bool GATHER, bool ALIGN_EPI, bool SP2, bool FP8>
; __device__ __forceinline__ void gemm_phase(LAS unsigned char* lds, const Gemm g, const Sched& S, const Epi& E) {
;     ...
;             PG8_LDB(B0, 0, 0); PG8_LDB(B1, 0, 1); PG8_SCHED; PG8_LDA(At, 0, 0); PG8_STAGE_A(PG8_SA(1, 1), a1, vA1);
;             PG8_WAIT_V(8); PG8_WAIT_L(0); PG8_BAR; PG8_MMA(0, 0, At, B0); PG8_MMA(0, 1, At, B1); PG8_BAR; PG8_SCHED;
;             PG8_LDA(At, 0, 1); PG8_STAGE_B(PG8_SB(0, 0), b2); PG8_STAGE_B(PG8_SB(0, 1), b2 + hstep); PG8_STAGE_A(PG8_SA(0, 0), a2, va20);
;             PG8_WAIT_V(8); PG8_WAIT_L(0); PG8_BAR; PG8_MMA(1, 0, At, B0); PG8_MMA(1, 1, At, B1); PG8_BAR; PG8_SCHED;
.LBB0_931:
	s_and_b64 s[8:9], s[2:3], exec
	s_cselect_b32 s8, 0, s6
	s_add_i32 s9, s80, s6
	s_or_b32 s7, s8, 0x80
	s_and_b64 s[2:3], s[2:3], exec
	s_cselect_b32 s2, s25, s9
	s_add_i32 s3, s6, 0xffffff80
	s_mov_b32 s66, s62
	s_mov_b32 s67, s63
	v_add_u32_e32 v14, 0x10000, v176
	ds_read_b128 v[2:5], v14
	ds_read_b128 v[6:9], v14 offset:1024
	ds_read_b128 v[10:13], v14 offset:2048
	ds_read_b128 v[14:17], v14 offset:3072
	v_add_u32_e32 v191, 0x14000, v176
	ds_read_b128 v[224:227], v191
	ds_read_b128 v[228:231], v191 offset:1024
	ds_read_b128 v[232:235], v191 offset:2048
	ds_read_b128 v[236:239], v191 offset:3072
	ds_read_b128 v[192:195], v177
	ds_read_b128 v[196:199], v177 offset:1024
	ds_read_b128 v[200:203], v177 offset:2048
	ds_read_b128 v[204:207], v177 offset:3072
	ds_read_b128 v[208:211], v177 offset:4096
	ds_read_b128 v[212:215], v177 offset:5120
	ds_read_b128 v[216:219], v177 offset:6144
	ds_read_b128 v[220:223], v177 offset:7168
	s_mov_b32 m0, s51
	s_nop 0
	buffer_load_dwordx4 v184, s[60:63], s3 offen lds
	s_mov_b32 m0, s52
	s_nop 0
	buffer_load_dwordx4 v186, s[60:63], s3 offen lds
	s_waitcnt vmcnt(8)
	s_waitcnt lgkmcnt(0)
	s_barrier
	s_setprio 1
	v_mfma_f32_16x16x128_f8f6f4 v[158:161], v[2:9], v[192:199], v[158:161]
	v_mfma_f32_16x16x128_f8f6f4 v[154:157], v[10:17], v[192:199], v[154:157]
	v_mfma_f32_16x16x128_f8f6f4 v[142:145], v[2:9], v[200:207], v[142:145]
	v_mfma_f32_16x16x128_f8f6f4 v[138:141], v[10:17], v[200:207], v[138:141]
	v_mfma_f32_16x16x128_f8f6f4 v[126:129], v[2:9], v[208:215], v[126:129]
	v_mfma_f32_16x16x128_f8f6f4 v[122:125], v[10:17], v[208:215], v[122:125]
	v_mfma_f32_16x16x128_f8f6f4 v[110:113], v[2:9], v[216:223], v[110:113]
	v_mfma_f32_16x16x128_f8f6f4 v[106:109], v[10:17], v[216:223], v[106:109]
	v_mfma_f32_16x16x128_f8f6f4 v[150:153], v[224:231], v[192:199], v[150:153]
	v_mfma_f32_16x16x128_f8f6f4 v[146:149], v[232:239], v[192:199], v[146:149]
	v_mfma_f32_16x16x128_f8f6f4 v[134:137], v[224:231], v[200:207], v[134:137]
	v_mfma_f32_16x16x128_f8f6f4 v[130:133], v[232:239], v[200:207], v[130:133]
	v_mfma_f32_16x16x128_f8f6f4 v[118:121], v[224:231], v[208:215], v[118:121]
	v_mfma_f32_16x16x128_f8f6f4 v[114:117], v[232:239], v[208:215], v[114:117]
	v_mfma_f32_16x16x128_f8f6f4 v[102:105], v[224:231], v[216:223], v[102:105]
	v_mfma_f32_16x16x128_f8f6f4 v[98:101], v[232:239], v[216:223], v[98:101]
	s_setprio 0
	s_barrier
	ds_read_b128 v[192:195], v177 offset:16384
	ds_read_b128 v[196:199], v177 offset:17408
	ds_read_b128 v[200:203], v177 offset:18432
	ds_read_b128 v[204:207], v177 offset:19456
	ds_read_b128 v[208:211], v177 offset:20480
	ds_read_b128 v[212:215], v177 offset:21504
	ds_read_b128 v[216:219], v177 offset:22528
	ds_read_b128 v[220:223], v177 offset:23552
	s_mov_b32 m0, s37
	s_nop 0
	buffer_load_dwordx4 v173, s[64:67], s2 offen lds
	s_mov_b32 m0, s38
	s_nop 0
	buffer_load_dwordx4 v174, s[64:67], s2 offen lds
	s_add_i32 s3, s2, 0x40000
	s_mov_b32 m0, s40
	s_nop 0
	buffer_load_dwordx4 v173, s[64:67], s3 offen lds
	s_mov_b32 m0, s41
	s_nop 0
	buffer_load_dwordx4 v174, s[64:67], s3 offen lds
	s_mov_b32 m0, s36
	s_nop 0
	buffer_load_dwordx4 v187, s[60:63], s8 offen lds
	s_mov_b32 m0, s39
	s_nop 0
	buffer_load_dwordx4 v188, s[60:63], s8 offen lds
	s_waitcnt vmcnt(8)
	s_waitcnt lgkmcnt(0)
	s_barrier
	s_setprio 1
	v_mfma_f32_16x16x128_f8f6f4 v[94:97], v[2:9], v[192:199], v[94:97]
	v_mfma_f32_16x16x128_f8f6f4 v[90:93], v[10:17], v[192:199], v[90:93]
	v_mfma_f32_16x16x128_f8f6f4 v[78:81], v[2:9], v[200:207], v[78:81]
	v_mfma_f32_16x16x128_f8f6f4 v[74:77], v[10:17], v[200:207], v[74:77]
	v_mfma_f32_16x16x128_f8f6f4 v[62:65], v[2:9], v[208:215], v[62:65]
	v_mfma_f32_16x16x128_f8f6f4 v[58:61], v[10:17], v[208:215], v[58:61]
	v_mfma_f32_16x16x128_f8f6f4 v[46:49], v[2:9], v[216:223], v[46:49]
	v_mfma_f32_16x16x128_f8f6f4 v[42:45], v[10:17], v[216:223], v[42:45]
	v_mfma_f32_16x16x128_f8f6f4 v[86:89], v[224:231], v[192:199], v[86:89]
	v_mfma_f32_16x16x128_f8f6f4 v[82:85], v[232:239], v[192:199], v[82:85]
	v_mfma_f32_16x16x128_f8f6f4 v[70:73], v[224:231], v[200:207], v[70:73]
	v_mfma_f32_16x16x128_f8f6f4 v[66:69], v[232:239], v[200:207], v[66:69]
	v_mfma_f32_16x16x128_f8f6f4 v[54:57], v[224:231], v[208:215], v[54:57]
	v_mfma_f32_16x16x128_f8f6f4 v[50:53], v[232:239], v[208:215], v[50:53]
	v_mfma_f32_16x16x128_f8f6f4 v[38:41], v[224:231], v[216:223], v[38:41]
	v_mfma_f32_16x16x128_f8f6f4 v[34:37], v[232:239], v[216:223], v[34:37]
	s_setprio 0
	s_barrier
; #define PG8_STAGE_A(bufoff, soff, voff) do { _Pragma("unroll") for (int _i = 0; _i < 2; ++_i) \
;         __builtin_amdgcn_raw_ptr_buffer_load_lds(rsA, (LAS void*)(lds + (bufoff) + ldsw + _i * 8192), 16, (voff)[_i], (soff), 0, 0); } while (0)
; #define PG8_STAGE_B(bufoff, soff) do { _Pragma("unroll") for (int _i = 0; _i < 2; ++_i) \
;         __builtin_amdgcn_raw_ptr_buffer_load_lds(rsB, (LAS void*)(lds + (bufoff) + ldsw + _i * 8192), 16, voffB[_i], (soff), 0, 0); } while (0)
; #define PG8_LDA(dst, b, h) do { _Pragma("unroll") for (int m = 0; m < 4; ++m) dst[m] = PG8_LD8(lds + PG8_SA(b, h) + aoff + m * 2048); } while (0)
; #define PG8_LDB(dst, b, h) do { _Pragma("unroll") for (int n = 0; n < 2; ++n) dst[n] = PG8_LD8(lds + PG8_SB(b, h) + boff + n * 2048); } while (0)
; #define PG8_WAIT_V(n) asm volatile("s_waitcnt vmcnt(" #n ")" ::: "memory")
; #define PG8_WAIT_L(n) asm volatile("s_waitcnt lgkmcnt(" #n ")" ::: "memory")
; #define PG8_BAR __builtin_amdgcn_s_barrier()
; #define PG8_SCHED __builtin_amdgcn_sched_barrier(0)
; template <class Epi, class Sched, bool GATHER, bool ALIGN_EPI, bool SP2, bool FP8>
; __device__ __forceinline__ void gemm_phase(LAS unsigned char* lds, const Gemm g, const Sched& S, const Epi& E) {
;     ...
;             PG8_LDB(B0, 1, 0); PG8_LDB(B1, 1, 1); PG8_SCHED; PG8_LDA(At, 1, 0); PG8_STAGE_A(PG8_SA(0, 1), a2, va21);
;             PG8_WAIT_V(8); PG8_WAIT_L(0); PG8_BAR; PG8_MMA(0, 0, At, B0); PG8_MMA(0, 1, At, B1); PG8_BAR; PG8_SCHED;
;             PG8_LDA(At, 1, 1); PG8_STAGE_B(PG8_SB(1, 0), b3); PG8_STAGE_B(PG8_SB(1, 1), b3 + hstep); PG8_STAGE_A(PG8_SA(1, 0), a3, va20);
;             PG8_WAIT_V(8); PG8_WAIT_L(0); PG8_BAR; PG8_MMA(1, 0, At, B0); PG8_MMA(1, 1, At, B1); PG8_BAR; PG8_SCHED;
	v_add_u32_e32 v14, 0x18000, v176
	ds_read_b128 v[2:5], v14
	ds_read_b128 v[6:9], v14 offset:1024
	ds_read_b128 v[10:13], v14 offset:2048
	ds_read_b128 v[14:17], v14 offset:3072
	v_add_u32_e32 v191, 0x1c000, v176
	ds_read_b128 v[224:227], v191
	ds_read_b128 v[228:231], v191 offset:1024
	ds_read_b128 v[232:235], v191 offset:2048
	ds_read_b128 v[236:239], v191 offset:3072
	ds_read_b128 v[192:195], v177 offset:32768
	ds_read_b128 v[196:199], v177 offset:33792
	ds_read_b128 v[200:203], v177 offset:34816
	ds_read_b128 v[204:207], v177 offset:35840
	ds_read_b128 v[208:211], v177 offset:36864
	ds_read_b128 v[212:215], v177 offset:37888
	ds_read_b128 v[216:219], v177 offset:38912
	ds_read_b128 v[220:223], v177 offset:39936
	s_mov_b32 m0, s42
	s_nop 0
	buffer_load_dwordx4 v190, s[60:63], s8 offen lds
	s_mov_b32 m0, s43
	s_nop 0
	buffer_load_dwordx4 v189, s[60:63], s8 offen lds
	s_waitcnt vmcnt(8)
	s_waitcnt lgkmcnt(0)
	s_barrier
	s_setprio 1
	v_mfma_f32_16x16x128_f8f6f4 v[158:161], v[2:9], v[192:199], v[158:161]
	v_mfma_f32_16x16x128_f8f6f4 v[154:157], v[10:17], v[192:199], v[154:157]
	v_mfma_f32_16x16x128_f8f6f4 v[142:145], v[2:9], v[200:207], v[142:145]
	v_mfma_f32_16x16x128_f8f6f4 v[138:141], v[10:17], v[200:207], v[138:141]
	v_mfma_f32_16x16x128_f8f6f4 v[126:129], v[2:9], v[208:215], v[126:129]
	v_mfma_f32_16x16x128_f8f6f4 v[122:125], v[10:17], v[208:215], v[122:125]
	v_mfma_f32_16x16x128_f8f6f4 v[110:113], v[2:9], v[216:223], v[110:113]
	v_mfma_f32_16x16x128_f8f6f4 v[106:109], v[10:17], v[216:223], v[106:109]
	v_mfma_f32_16x16x128_f8f6f4 v[150:153], v[224:231], v[192:199], v[150:153]
	v_mfma_f32_16x16x128_f8f6f4 v[146:149], v[232:239], v[192:199], v[146:149]
	v_mfma_f32_16x16x128_f8f6f4 v[134:137], v[224:231], v[200:207], v[134:137]
	v_mfma_f32_16x16x128_f8f6f4 v[130:133], v[232:239], v[200:207], v[130:133]
	v_mfma_f32_16x16x128_f8f6f4 v[118:121], v[224:231], v[208:215], v[118:121]
	v_mfma_f32_16x16x128_f8f6f4 v[114:117], v[232:239], v[208:215], v[114:117]
	v_mfma_f32_16x16x128_f8f6f4 v[102:105], v[224:231], v[216:223], v[102:105]
	v_mfma_f32_16x16x128_f8f6f4 v[98:101], v[232:239], v[216:223], v[98:101]
	s_setprio 0
	s_barrier
	ds_read_b128 v[190:193], v177 offset:49152
	ds_read_b128 v[194:197], v177 offset:50176
	ds_read_b128 v[198:201], v177 offset:51200
	ds_read_b128 v[202:205], v177 offset:52224
	ds_read_b128 v[206:209], v177 offset:53248
	ds_read_b128 v[210:213], v177 offset:54272
	ds_read_b128 v[214:217], v177 offset:55296
	ds_read_b128 v[218:221], v177 offset:56320
	s_or_b32 s2, s2, 0x80
	s_mov_b32 m0, s44
	s_nop 0
	buffer_load_dwordx4 v173, s[64:67], s2 offen lds
	s_mov_b32 m0, s45
	s_nop 0
	buffer_load_dwordx4 v174, s[64:67], s2 offen lds
	s_add_i32 s3, s2, 0x40000
	s_mov_b32 m0, s48
	s_nop 0
	buffer_load_dwordx4 v173, s[64:67], s3 offen lds
	s_mov_b32 m0, s49
	s_nop 0
	buffer_load_dwordx4 v174, s[64:67], s3 offen lds
	s_mov_b32 m0, s46
	s_nop 0
	buffer_load_dwordx4 v187, s[60:63], s7 offen lds
	s_mov_b32 m0, s47
	s_nop 0
	buffer_load_dwordx4 v188, s[60:63], s7 offen lds
	s_waitcnt vmcnt(8)
	s_waitcnt lgkmcnt(0)
	s_barrier
	s_setprio 1
	v_mfma_f32_16x16x128_f8f6f4 v[94:97], v[2:9], v[190:197], v[94:97]
	v_mfma_f32_16x16x128_f8f6f4 v[90:93], v[10:17], v[190:197], v[90:93]
	v_mfma_f32_16x16x128_f8f6f4 v[78:81], v[2:9], v[198:205], v[78:81]
	v_mfma_f32_16x16x128_f8f6f4 v[74:77], v[10:17], v[198:205], v[74:77]
	v_mfma_f32_16x16x128_f8f6f4 v[62:65], v[2:9], v[206:213], v[62:65]
	v_mfma_f32_16x16x128_f8f6f4 v[58:61], v[10:17], v[206:213], v[58:61]
	v_mfma_f32_16x16x128_f8f6f4 v[46:49], v[2:9], v[214:221], v[46:49]
	v_mfma_f32_16x16x128_f8f6f4 v[42:45], v[10:17], v[214:221], v[42:45]
	v_mfma_f32_16x16x128_f8f6f4 v[86:89], v[224:231], v[190:197], v[86:89]
	v_mfma_f32_16x16x128_f8f6f4 v[82:85], v[232:239], v[190:197], v[82:85]
	v_mfma_f32_16x16x128_f8f6f4 v[70:73], v[224:231], v[198:205], v[70:73]
	v_mfma_f32_16x16x128_f8f6f4 v[66:69], v[232:239], v[198:205], v[66:69]
	v_mfma_f32_16x16x128_f8f6f4 v[54:57], v[224:231], v[206:213], v[54:57]
	v_mfma_f32_16x16x128_f8f6f4 v[50:53], v[232:239], v[206:213], v[50:53]
	v_mfma_f32_16x16x128_f8f6f4 v[38:41], v[224:231], v[214:221], v[38:41]
	v_mfma_f32_16x16x128_f8f6f4 v[34:37], v[232:239], v[214:221], v[34:37]
	s_setprio 0
	s_add_i32 s5, s5, 2
	s_addk_i32 s6, 0x100
	s_cmp_gt_u32 s5, 13
	s_barrier
	s_cbranch_scc1 .LBB0_934
